# speedup vs baseline: 1.0071x; 1.0071x over previous
.Lk4_st4_7:
	v_add_u32_e32 v128, s17, v118
	s_nop 1
	v_readfirstlane_b32 s14, v128
	s_mov_b32 m0, s14
	s_nop 0
	global_load_lds_dwordx4 v[102:103], off nt
	v_add_u32_e32 v128, s17, v90
	s_nop 1
	v_readfirstlane_b32 s14, v128
	s_mov_b32 m0, s14
	s_nop 0
	global_load_lds_dwordx4 v[104:105], off nt
	v_add_u32_e32 v128, s17, v91
	s_nop 1
	v_readfirstlane_b32 s14, v128
	s_mov_b32 m0, s14
	s_nop 0
	global_load_lds_dwordx4 v[108:109], off nt
	v_add_u32_e32 v128, s17, v119
	s_nop 1
	v_readfirstlane_b32 s14, v128
	s_mov_b32 m0, s14
	s_nop 0
	global_load_lds_dwordx4 v[112:113], off nt
	v_add_u32_e32 v128, s16, v118
	s_nop 1
	v_readfirstlane_b32 s14, v128
	s_mov_b32 m0, s14
	s_nop 0
	global_load_lds_dwordx4 v[0:1], off nt
	v_mfma_f32_16x16x32_f16 a[0:3], v[70:73], v[82:85], a[0:3]
	ds_read_b128 v[14:17], v152
	v_mfma_f32_16x16x32_f16 a[4:7], v[70:73], v[86:89], a[4:7]
	ds_read_b128 v[18:21], v154
	v_mfma_f32_16x16x32_f16 a[12:15], v[66:69], v[82:85], a[12:15]
	ds_read_b128 v[42:45], v164
	v_mfma_f32_16x16x32_f16 a[16:19], v[66:69], v[86:89], a[16:19]
	ds_read_b128 v[38:41], v164 offset:1024
	v_mfma_f32_16x16x32_f16 a[28:31], v[58:61], v[82:85], a[28:31]
	ds_read_b128 v[34:37], v164 offset:2048
	v_mfma_f32_16x16x32_f16 a[60:63], v[58:61], v[86:89], a[60:63]
	ds_read_b128 v[30:33], v164 offset:3072
	v_mfma_f32_16x16x32_f16 a[8:11], v[54:57], v[82:85], a[8:11]
	ds_read_b128 v[26:29], v164 offset:4096
	v_mfma_f32_16x16x32_f16 a[20:23], v[54:57], v[86:89], a[20:23]
	ds_read_b128 v[22:25], v164 offset:5120
	v_mfma_f32_16x16x32_f16 a[24:27], v[46:49], v[82:85], a[24:27]
	ds_read_b128 v[10:13], v164 offset:6144
	v_mfma_f32_16x16x32_f16 a[36:39], v[46:49], v[86:89], a[36:39]
	ds_read_b128 v[6:9], v164 offset:7168
	v_mfma_f32_16x16x32_f16 a[44:47], v[50:53], v[82:85], a[44:47]
	ds_read_b128 v[2:5], v164 offset:8192
	v_mfma_f32_16x16x32_f16 a[64:67], v[50:53], v[86:89], a[64:67]
	v_mfma_f32_16x16x32_f16 a[32:35], v[62:65], v[82:85], a[32:35]
	v_mfma_f32_16x16x32_f16 a[40:43], v[62:65], v[86:89], a[40:43]
	v_mfma_f32_16x16x32_f16 a[48:51], v[74:77], v[82:85], a[48:51]
	v_mfma_f32_16x16x32_f16 a[52:55], v[74:77], v[86:89], a[52:55]
	v_mfma_f32_16x16x32_f16 a[56:59], v[78:81], v[82:85], a[56:59]
	v_mfma_f32_16x16x32_f16 a[68:71], v[78:81], v[86:89], a[68:71]
	s_waitcnt lgkmcnt(8)
	v_mfma_f32_16x16x32_f16 a[0:3], v[42:45], v[14:17], a[0:3]
	ds_read_b128 v[82:85], v153
	v_mfma_f32_16x16x32_f16 a[4:7], v[42:45], v[18:21], a[4:7]
	ds_read_b128 v[86:89], v155
	s_waitcnt lgkmcnt(9)
	v_mfma_f32_16x16x32_f16 a[12:15], v[38:41], v[14:17], a[12:15]
	ds_read_b128 v[70:73], v164 offset:9216
	v_mfma_f32_16x16x32_f16 a[16:19], v[38:41], v[18:21], a[16:19]
	ds_read_b128 v[66:69], v164 offset:10240
	s_waitcnt lgkmcnt(10)
	v_mfma_f32_16x16x32_f16 a[28:31], v[34:37], v[14:17], a[28:31]
	ds_read_b128 v[58:61], v164 offset:11264
	v_mfma_f32_16x16x32_f16 a[60:63], v[34:37], v[18:21], a[60:63]
	ds_read_b128 v[54:57], v164 offset:12288
	s_waitcnt lgkmcnt(11)
	v_mfma_f32_16x16x32_f16 a[8:11], v[30:33], v[14:17], a[8:11]
	ds_read_b128 v[46:49], v164 offset:13312
	v_mfma_f32_16x16x32_f16 a[20:23], v[30:33], v[18:21], a[20:23]
	ds_read_b128 v[50:53], v164 offset:14336
	s_waitcnt lgkmcnt(12)
	v_mfma_f32_16x16x32_f16 a[24:27], v[26:29], v[14:17], a[24:27]
	ds_read_b128 v[62:65], v164 offset:15360
	v_mfma_f32_16x16x32_f16 a[36:39], v[26:29], v[18:21], a[36:39]
	ds_read_b128 v[74:77], v164 offset:16384
	s_waitcnt lgkmcnt(13)
	v_mfma_f32_16x16x32_f16 a[44:47], v[22:25], v[14:17], a[44:47]
	ds_read_b128 v[78:81], v164 offset:17408
	v_mfma_f32_16x16x32_f16 a[64:67], v[22:25], v[18:21], a[64:67]
	s_waitcnt lgkmcnt(13)
	v_mfma_f32_16x16x32_f16 a[32:35], v[10:13], v[14:17], a[32:35]
	v_mfma_f32_16x16x32_f16 a[40:43], v[10:13], v[18:21], a[40:43]
	s_waitcnt lgkmcnt(12)
	v_mfma_f32_16x16x32_f16 a[48:51], v[6:9], v[14:17], a[48:51]
	v_mfma_f32_16x16x32_f16 a[52:55], v[6:9], v[18:21], a[52:55]
	s_waitcnt lgkmcnt(11)
	v_mfma_f32_16x16x32_f16 a[56:59], v[2:5], v[14:17], a[56:59]
	v_mfma_f32_16x16x32_f16 a[68:71], v[2:5], v[18:21], a[68:71]
	s_waitcnt lgkmcnt(8)
	v_mfma_f32_16x16x32_f16 a[0:3], v[70:73], v[82:85], a[0:3]
	ds_read_b128 v[14:17], v156
	v_mfma_f32_16x16x32_f16 a[4:7], v[70:73], v[86:89], a[4:7]
	ds_read_b128 v[18:21], v158
	s_waitcnt lgkmcnt(9)
	v_mfma_f32_16x16x32_f16 a[12:15], v[66:69], v[82:85], a[12:15]
	ds_read_b128 v[42:45], v165
	v_mfma_f32_16x16x32_f16 a[16:19], v[66:69], v[86:89], a[16:19]
	ds_read_b128 v[38:41], v165 offset:1024
	s_waitcnt lgkmcnt(10)
	v_mfma_f32_16x16x32_f16 a[28:31], v[58:61], v[82:85], a[28:31]
	ds_read_b128 v[34:37], v165 offset:2048
	v_mfma_f32_16x16x32_f16 a[60:63], v[58:61], v[86:89], a[60:63]
	ds_read_b128 v[30:33], v165 offset:3072
	s_waitcnt lgkmcnt(11)
	v_mfma_f32_16x16x32_f16 a[8:11], v[54:57], v[82:85], a[8:11]
	ds_read_b128 v[26:29], v165 offset:4096
	v_mfma_f32_16x16x32_f16 a[20:23], v[54:57], v[86:89], a[20:23]
	ds_read_b128 v[22:25], v165 offset:5120
	s_waitcnt lgkmcnt(12)
	v_mfma_f32_16x16x32_f16 a[24:27], v[46:49], v[82:85], a[24:27]
	ds_read_b128 v[10:13], v165 offset:6144
	v_mfma_f32_16x16x32_f16 a[36:39], v[46:49], v[86:89], a[36:39]
	ds_read_b128 v[6:9], v165 offset:7168
	s_waitcnt lgkmcnt(13)
	v_mfma_f32_16x16x32_f16 a[44:47], v[50:53], v[82:85], a[44:47]
	ds_read_b128 v[2:5], v165 offset:8192
	v_mfma_f32_16x16x32_f16 a[64:67], v[50:53], v[86:89], a[64:67]
	s_waitcnt lgkmcnt(13)
	v_mfma_f32_16x16x32_f16 a[32:35], v[62:65], v[82:85], a[32:35]
	v_mfma_f32_16x16x32_f16 a[40:43], v[62:65], v[86:89], a[40:43]
	s_waitcnt lgkmcnt(12)
	v_mfma_f32_16x16x32_f16 a[48:51], v[74:77], v[82:85], a[48:51]
	v_mfma_f32_16x16x32_f16 a[52:55], v[74:77], v[86:89], a[52:55]
	s_waitcnt lgkmcnt(11)
	v_mfma_f32_16x16x32_f16 a[56:59], v[78:81], v[82:85], a[56:59]
	v_mfma_f32_16x16x32_f16 a[68:71], v[78:81], v[86:89], a[68:71]
	s_waitcnt lgkmcnt(8)
	v_mfma_f32_16x16x32_f16 a[0:3], v[42:45], v[14:17], a[0:3]
	ds_read_b128 v[82:85], v157
	v_mfma_f32_16x16x32_f16 a[4:7], v[42:45], v[18:21], a[4:7]
	ds_read_b128 v[86:89], v159
	s_waitcnt lgkmcnt(9)
	v_mfma_f32_16x16x32_f16 a[12:15], v[38:41], v[14:17], a[12:15]
	ds_read_b128 v[70:73], v165 offset:9216
	v_mfma_f32_16x16x32_f16 a[16:19], v[38:41], v[18:21], a[16:19]
	ds_read_b128 v[66:69], v165 offset:10240
	s_waitcnt lgkmcnt(10)
	v_mfma_f32_16x16x32_f16 a[28:31], v[34:37], v[14:17], a[28:31]
	ds_read_b128 v[58:61], v165 offset:11264
	v_mfma_f32_16x16x32_f16 a[60:63], v[34:37], v[18:21], a[60:63]
	ds_read_b128 v[54:57], v165 offset:12288
	s_waitcnt lgkmcnt(11)
	v_mfma_f32_16x16x32_f16 a[8:11], v[30:33], v[14:17], a[8:11]
	ds_read_b128 v[46:49], v165 offset:13312
	v_mfma_f32_16x16x32_f16 a[20:23], v[30:33], v[18:21], a[20:23]
	ds_read_b128 v[50:53], v165 offset:14336
	s_waitcnt lgkmcnt(12)
	v_mfma_f32_16x16x32_f16 a[24:27], v[26:29], v[14:17], a[24:27]
	ds_read_b128 v[62:65], v165 offset:15360
	v_mfma_f32_16x16x32_f16 a[36:39], v[26:29], v[18:21], a[36:39]
	ds_read_b128 v[74:77], v165 offset:16384
	s_waitcnt lgkmcnt(13)
	v_mfma_f32_16x16x32_f16 a[44:47], v[22:25], v[14:17], a[44:47]
	ds_read_b128 v[78:81], v165 offset:17408
	v_mfma_f32_16x16x32_f16 a[64:67], v[22:25], v[18:21], a[64:67]
	s_waitcnt lgkmcnt(13)
	v_mfma_f32_16x16x32_f16 a[32:35], v[10:13], v[14:17], a[32:35]
	v_mfma_f32_16x16x32_f16 a[40:43], v[10:13], v[18:21], a[40:43]
	s_waitcnt lgkmcnt(12)
	v_mfma_f32_16x16x32_f16 a[48:51], v[6:9], v[14:17], a[48:51]
	v_mfma_f32_16x16x32_f16 a[52:55], v[6:9], v[18:21], a[52:55]
	s_waitcnt lgkmcnt(11)
	v_mfma_f32_16x16x32_f16 a[56:59], v[2:5], v[14:17], a[56:59]
	v_mfma_f32_16x16x32_f16 a[68:71], v[2:5], v[18:21], a[68:71]
	s_waitcnt vmcnt(5) lgkmcnt(0)
	s_barrier
	s_add_u32 s52, s50, 0x24000
	s_addc_u32 s53, s51, 0
	s_add_i32 m0, s42, 0xc600
	s_nop 0
	global_load_lds_dwordx4 v137, s[52:53]
	s_add_i32 m0, s43, 0xc600
	s_nop 0
	global_load_lds_dwordx4 v138, s[52:53]
	s_cmp_lt_u32 s42, 0x800
	s_cbranch_scc0 .Lk4_st6_8
	s_add_i32 m0, s44, 0xc600
	s_nop 0
	global_load_lds_dwordx4 v139, s[52:53]
.Lk4_st6_8:
	s_add_u32 s52, s10, 0x800000
	s_addc_u32 s53, s11, 0
	v_lshlrev_b64 v[130:131], 2, v[94:95]
	v_readfirstlane_b32 s14, v118
	v_lshl_add_u64 v[128:129], s[52:53], 0, v[130:131]
	s_mov_b32 m0, s14
	s_nop 0
	global_load_lds_dwordx4 v[128:129], off nt
	v_lshlrev_b64 v[130:131], 2, v[96:97]
	v_readfirstlane_b32 s14, v90
	v_lshl_add_u64 v[128:129], s[52:53], 0, v[130:131]
	s_mov_b32 m0, s14
	s_nop 0
	global_load_lds_dwordx4 v[128:129], off nt
	v_mfma_f32_16x16x32_f16 a[0:3], v[70:73], v[82:85], a[0:3]
	ds_read_b128 v[14:17], v158
	v_mfma_f32_16x16x32_f16 a[4:7], v[70:73], v[86:89], a[4:7]
	ds_read_b128 v[18:21], v160
	v_mfma_f32_16x16x32_f16 a[12:15], v[66:69], v[82:85], a[12:15]
	ds_read_b128 v[42:45], v168
	v_mfma_f32_16x16x32_f16 a[16:19], v[66:69], v[86:89], a[16:19]
	ds_read_b128 v[38:41], v168 offset:1024
	v_mfma_f32_16x16x32_f16 a[28:31], v[58:61], v[82:85], a[28:31]
	ds_read_b128 v[34:37], v168 offset:2048
	v_mfma_f32_16x16x32_f16 a[60:63], v[58:61], v[86:89], a[60:63]
	ds_read_b128 v[30:33], v168 offset:3072
	v_mfma_f32_16x16x32_f16 a[8:11], v[54:57], v[82:85], a[8:11]
	ds_read_b128 v[26:29], v168 offset:4096
	v_mfma_f32_16x16x32_f16 a[20:23], v[54:57], v[86:89], a[20:23]
	ds_read_b128 v[22:25], v168 offset:5120
	v_mfma_f32_16x16x32_f16 a[24:27], v[46:49], v[82:85], a[24:27]
	ds_read_b128 v[10:13], v168 offset:6144
	v_mfma_f32_16x16x32_f16 a[36:39], v[46:49], v[86:89], a[36:39]
	ds_read_b128 v[6:9], v168 offset:7168
	v_mfma_f32_16x16x32_f16 a[44:47], v[50:53], v[82:85], a[44:47]
	ds_read_b128 v[2:5], v168 offset:8192
	v_mfma_f32_16x16x32_f16 a[64:67], v[50:53], v[86:89], a[64:67]
	v_mfma_f32_16x16x32_f16 a[32:35], v[62:65], v[82:85], a[32:35]
	v_mfma_f32_16x16x32_f16 a[40:43], v[62:65], v[86:89], a[40:43]
	v_mfma_f32_16x16x32_f16 a[48:51], v[74:77], v[82:85], a[48:51]
	v_mfma_f32_16x16x32_f16 a[52:55], v[74:77], v[86:89], a[52:55]
	v_mfma_f32_16x16x32_f16 a[56:59], v[78:81], v[82:85], a[56:59]
	v_mfma_f32_16x16x32_f16 a[68:71], v[78:81], v[86:89], a[68:71]
	s_waitcnt lgkmcnt(8)
	v_mfma_f32_16x16x32_f16 a[0:3], v[42:45], v[14:17], a[0:3]
	ds_read_b128 v[82:85], v159
	v_mfma_f32_16x16x32_f16 a[4:7], v[42:45], v[18:21], a[4:7]
	ds_read_b128 v[86:89], v161
	s_waitcnt lgkmcnt(9)
	v_mfma_f32_16x16x32_f16 a[12:15], v[38:41], v[14:17], a[12:15]
	ds_read_b128 v[70:73], v168 offset:9216
	v_mfma_f32_16x16x32_f16 a[16:19], v[38:41], v[18:21], a[16:19]
	ds_read_b128 v[66:69], v168 offset:10240
	s_waitcnt lgkmcnt(10)
	v_mfma_f32_16x16x32_f16 a[28:31], v[34:37], v[14:17], a[28:31]
	ds_read_b128 v[58:61], v168 offset:11264
	v_mfma_f32_16x16x32_f16 a[60:63], v[34:37], v[18:21], a[60:63]
	ds_read_b128 v[54:57], v168 offset:12288
	s_waitcnt lgkmcnt(11)
	v_mfma_f32_16x16x32_f16 a[8:11], v[30:33], v[14:17], a[8:11]
	ds_read_b128 v[46:49], v168 offset:13312
	v_mfma_f32_16x16x32_f16 a[20:23], v[30:33], v[18:21], a[20:23]
	ds_read_b128 v[50:53], v168 offset:14336
	s_waitcnt lgkmcnt(12)
	v_mfma_f32_16x16x32_f16 a[24:27], v[26:29], v[14:17], a[24:27]
	ds_read_b128 v[62:65], v168 offset:15360
	v_mfma_f32_16x16x32_f16 a[36:39], v[26:29], v[18:21], a[36:39]
	ds_read_b128 v[74:77], v168 offset:16384
	s_waitcnt lgkmcnt(13)
	v_mfma_f32_16x16x32_f16 a[44:47], v[22:25], v[14:17], a[44:47]
	ds_read_b128 v[78:81], v168 offset:17408
	v_mfma_f32_16x16x32_f16 a[64:67], v[22:25], v[18:21], a[64:67]
	s_waitcnt lgkmcnt(13)
	v_mfma_f32_16x16x32_f16 a[32:35], v[10:13], v[14:17], a[32:35]
	v_mfma_f32_16x16x32_f16 a[40:43], v[10:13], v[18:21], a[40:43]
	s_waitcnt lgkmcnt(12)
	v_mfma_f32_16x16x32_f16 a[48:51], v[6:9], v[14:17], a[48:51]
	v_mfma_f32_16x16x32_f16 a[52:55], v[6:9], v[18:21], a[52:55]
	s_waitcnt lgkmcnt(11)
	v_mfma_f32_16x16x32_f16 a[56:59], v[2:5], v[14:17], a[56:59]
	v_mfma_f32_16x16x32_f16 a[68:71], v[2:5], v[18:21], a[68:71]
	s_waitcnt vmcnt(2) lgkmcnt(0)
	s_barrier
	v_add_u32_e32 v128, s16, v90
	s_nop 1
	v_readfirstlane_b32 s14, v128
	s_mov_b32 m0, s14
	s_nop 0
	global_load_lds_dwordx4 v[106:107], off nt
	v_add_u32_e32 v128, s16, v91
	s_nop 1
	v_readfirstlane_b32 s14, v128
	s_mov_b32 m0, s14
	s_nop 0
	global_load_lds_dwordx4 v[110:111], off nt
	v_add_u32_e32 v128, s16, v119
	s_nop 1
	v_readfirstlane_b32 s14, v128
	s_mov_b32 m0, s14
	s_nop 0
	global_load_lds_dwordx4 v[114:115], off nt
	v_mfma_f32_16x16x32_f16 a[0:3], v[70:73], v[82:85], a[0:3]
	ds_read_b128 v[14:17], v160
	v_mfma_f32_16x16x32_f16 a[4:7], v[70:73], v[86:89], a[4:7]
	ds_read_b128 v[18:21], v162
	v_mfma_f32_16x16x32_f16 a[12:15], v[66:69], v[82:85], a[12:15]
	ds_read_b128 v[42:45], v164
	v_mfma_f32_16x16x32_f16 a[16:19], v[66:69], v[86:89], a[16:19]
	ds_read_b128 v[38:41], v164 offset:1024
	v_mfma_f32_16x16x32_f16 a[28:31], v[58:61], v[82:85], a[28:31]
	ds_read_b128 v[34:37], v164 offset:2048
	v_mfma_f32_16x16x32_f16 a[60:63], v[58:61], v[86:89], a[60:63]
	ds_read_b128 v[30:33], v164 offset:3072
	v_mfma_f32_16x16x32_f16 a[8:11], v[54:57], v[82:85], a[8:11]
	ds_read_b128 v[26:29], v164 offset:4096
	v_mfma_f32_16x16x32_f16 a[20:23], v[54:57], v[86:89], a[20:23]
	ds_read_b128 v[22:25], v164 offset:5120
	v_mfma_f32_16x16x32_f16 a[24:27], v[46:49], v[82:85], a[24:27]
	ds_read_b128 v[10:13], v164 offset:6144
	v_mfma_f32_16x16x32_f16 a[36:39], v[46:49], v[86:89], a[36:39]
	ds_read_b128 v[6:9], v164 offset:7168
	v_mfma_f32_16x16x32_f16 a[44:47], v[50:53], v[82:85], a[44:47]
	ds_read_b128 v[2:5], v164 offset:8192
	v_mfma_f32_16x16x32_f16 a[64:67], v[50:53], v[86:89], a[64:67]
	v_mfma_f32_16x16x32_f16 a[32:35], v[62:65], v[82:85], a[32:35]
	v_mfma_f32_16x16x32_f16 a[40:43], v[62:65], v[86:89], a[40:43]
	v_mfma_f32_16x16x32_f16 a[48:51], v[74:77], v[82:85], a[48:51]
	v_mfma_f32_16x16x32_f16 a[52:55], v[74:77], v[86:89], a[52:55]
	v_mfma_f32_16x16x32_f16 a[56:59], v[78:81], v[82:85], a[56:59]
	v_mfma_f32_16x16x32_f16 a[68:71], v[78:81], v[86:89], a[68:71]
	s_waitcnt lgkmcnt(8)
	v_mfma_f32_16x16x32_f16 a[0:3], v[42:45], v[14:17], a[0:3]
	ds_read_b128 v[82:85], v161
	v_mfma_f32_16x16x32_f16 a[4:7], v[42:45], v[18:21], a[4:7]
	ds_read_b128 v[86:89], v163
	s_waitcnt lgkmcnt(9)
	v_mfma_f32_16x16x32_f16 a[12:15], v[38:41], v[14:17], a[12:15]
	ds_read_b128 v[70:73], v164 offset:9216
	v_mfma_f32_16x16x32_f16 a[16:19], v[38:41], v[18:21], a[16:19]
	ds_read_b128 v[66:69], v164 offset:10240
	s_waitcnt lgkmcnt(10)
	v_mfma_f32_16x16x32_f16 a[28:31], v[34:37], v[14:17], a[28:31]
	ds_read_b128 v[58:61], v164 offset:11264
	v_mfma_f32_16x16x32_f16 a[60:63], v[34:37], v[18:21], a[60:63]
	ds_read_b128 v[54:57], v164 offset:12288
	s_waitcnt lgkmcnt(11)
	v_mfma_f32_16x16x32_f16 a[8:11], v[30:33], v[14:17], a[8:11]
	ds_read_b128 v[46:49], v164 offset:13312
	v_mfma_f32_16x16x32_f16 a[20:23], v[30:33], v[18:21], a[20:23]
	ds_read_b128 v[50:53], v164 offset:14336
	s_waitcnt lgkmcnt(12)
	v_mfma_f32_16x16x32_f16 a[24:27], v[26:29], v[14:17], a[24:27]
	ds_read_b128 v[62:65], v164 offset:15360
	v_mfma_f32_16x16x32_f16 a[36:39], v[26:29], v[18:21], a[36:39]
	ds_read_b128 v[74:77], v164 offset:16384
	s_waitcnt lgkmcnt(13)
	v_mfma_f32_16x16x32_f16 a[44:47], v[22:25], v[14:17], a[44:47]
	ds_read_b128 v[78:81], v164 offset:17408
	v_mfma_f32_16x16x32_f16 a[64:67], v[22:25], v[18:21], a[64:67]
	s_waitcnt lgkmcnt(13)
	v_mfma_f32_16x16x32_f16 a[32:35], v[10:13], v[14:17], a[32:35]
	v_mfma_f32_16x16x32_f16 a[40:43], v[10:13], v[18:21], a[40:43]
	s_waitcnt lgkmcnt(12)
	v_mfma_f32_16x16x32_f16 a[48:51], v[6:9], v[14:17], a[48:51]
	v_mfma_f32_16x16x32_f16 a[52:55], v[6:9], v[18:21], a[52:55]
	s_waitcnt lgkmcnt(11)
	v_mfma_f32_16x16x32_f16 a[56:59], v[2:5], v[14:17], a[56:59]
	v_mfma_f32_16x16x32_f16 a[68:71], v[2:5], v[18:21], a[68:71]
	s_waitcnt lgkmcnt(8)
	v_mfma_f32_16x16x32_f16 a[0:3], v[70:73], v[82:85], a[0:3]
	v_mfma_f32_16x16x32_f16 a[4:7], v[70:73], v[86:89], a[4:7]
	s_waitcnt lgkmcnt(9)
	v_mfma_f32_16x16x32_f16 a[12:15], v[66:69], v[82:85], a[12:15]
	v_mfma_f32_16x16x32_f16 a[16:19], v[66:69], v[86:89], a[16:19]
	s_waitcnt lgkmcnt(10)
	v_mfma_f32_16x16x32_f16 a[28:31], v[58:61], v[82:85], a[28:31]
	v_mfma_f32_16x16x32_f16 a[60:63], v[58:61], v[86:89], a[60:63]
	s_waitcnt lgkmcnt(11)
	v_mfma_f32_16x16x32_f16 a[8:11], v[54:57], v[82:85], a[8:11]
	v_mfma_f32_16x16x32_f16 a[20:23], v[54:57], v[86:89], a[20:23]
	s_waitcnt lgkmcnt(12)
	v_mfma_f32_16x16x32_f16 a[24:27], v[46:49], v[82:85], a[24:27]
	v_mfma_f32_16x16x32_f16 a[36:39], v[46:49], v[86:89], a[36:39]
	s_waitcnt lgkmcnt(13)
	v_mfma_f32_16x16x32_f16 a[44:47], v[50:53], v[82:85], a[44:47]
	v_mfma_f32_16x16x32_f16 a[64:67], v[50:53], v[86:89], a[64:67]
	s_waitcnt lgkmcnt(13)
	v_mfma_f32_16x16x32_f16 a[32:35], v[62:65], v[82:85], a[32:35]
	v_mfma_f32_16x16x32_f16 a[40:43], v[62:65], v[86:89], a[40:43]
	s_waitcnt lgkmcnt(12)
	v_mfma_f32_16x16x32_f16 a[48:51], v[74:77], v[82:85], a[48:51]
	v_mfma_f32_16x16x32_f16 a[52:55], v[74:77], v[86:89], a[52:55]
	s_waitcnt lgkmcnt(11)
	v_mfma_f32_16x16x32_f16 a[56:59], v[78:81], v[82:85], a[56:59]
	v_mfma_f32_16x16x32_f16 a[68:71], v[78:81], v[86:89], a[68:71]
	s_waitcnt lgkmcnt(0)
	s_setprio 0
